# nt cache policy also on the once-read f32 residual loads of the mix-out epilogue
# speedup vs baseline: 1.0091x; 1.0091x over previous
; #define PG8_LAS __attribute__((address_space(3)))
; __device__ __forceinline__ unsigned cvt_pk_bf16(float lo, float hi) { const f32x2c v = {lo, hi}; const bf16x2c b = __builtin_convertvector(v, bf16x2c); return __builtin_bit_cast(unsigned, b); }
;     __device__ __forceinline__ void operator()(const f32x4 (&acc)[2][2][4][2], const Unit& u, int wr, int wc, int fr, int fq) const {
;     ...
;             for (int m = 0; m < 4; ++m) { const size_t ro = (size_t)(row0 + ai * HALF + m * 16) * D + col0; float q = 0.f;
; #pragma unroll
;                 for (int bj = 0; bj < 2; ++bj) { const f32x4 v0 = acc[ai][bj][m][0] + *(const f32x4*)(R + ro + bj * HALF), v1 = acc[ai][bj][m][1] + *(const f32x4*)(R + ro + bj * HALF + 4);
;                     q += (v0[0] * v0[0] + v0[1] * v0[1]) + (v0[2] * v0[2] + v0[3] * v0[3]) + (v1[0] * v1[0] + v1[1] * v1[1]) + (v1[2] * v1[2] + v1[3] * v1[3]);
;                     u32x4 w; w.x = cvt_pk_bf16(v0[0], v0[1]); w.y = cvt_pk_bf16(v0[2], v0[3]); w.z = cvt_pk_bf16(v1[0], v1[1]); w.w = cvt_pk_bf16(v1[2], v1[3]);
;                     *(u32x4*)(O + ro + bj * HALF) = w; }
;                 q = rows_sum4(q);
;                 if (fq == 0) { PG8_LAS float* sp = ss + (ai * HALF + wr * 64 + m * 16 + fr) * 4 + wc; *sp += q; } }
.LBB0_2039:
	v_lshl_add_u32 v142, s16, 8, v144
	v_lshl_or_b32 v140, s17, 8, v146
	v_ashrrev_i32_e32 v143, 31, v142
	v_ashrrev_i32_e32 v141, 31, v140
	v_lshlrev_b64 v[150:151], 10, v[142:143]
	v_lshl_add_u64 v[142:143], v[150:151], 0, v[140:141]
	v_lshl_add_u64 v[140:141], v[142:143], 2, s[56:57]
	v_lshl_add_u64 v[142:143], v[142:143], 1, s[92:93]
	global_load_dwordx4 v[150:153], v[140:141], off nt
	global_load_dwordx4 v[154:157], v[140:141], off offset:16 nt
	global_load_dwordx4 v[158:161], v[140:141], off offset:512 nt
	global_load_dwordx4 v[162:165], v[140:141], off offset:528 nt
	s_mov_b64 s[98:99], 0x10000
	v_lshl_add_u64 v[202:203], v[140:141], 0, s[98:99]
	global_load_dwordx4 v[166:169], v[202:203], off nt
	global_load_dwordx4 v[170:173], v[202:203], off offset:16 nt
	global_load_dwordx4 v[174:177], v[202:203], off offset:512 nt
	global_load_dwordx4 v[178:181], v[202:203], off offset:528 nt
	s_mov_b64 s[98:99], 0x20000
	v_lshl_add_u64 v[202:203], v[140:141], 0, s[98:99]
	global_load_dwordx4 v[182:185], v[202:203], off nt
	global_load_dwordx4 v[186:189], v[202:203], off offset:16 nt
	global_load_dwordx4 v[190:193], v[202:203], off offset:512 nt
	global_load_dwordx4 v[198:201], v[202:203], off offset:528 nt
	s_waitcnt vmcnt(10)
	v_pk_add_f32 v[152:153], v[126:127], v[152:153]
	v_pk_add_f32 v[150:151], v[124:125], v[150:151]
	v_pk_add_f32 v[156:157], v[122:123], v[156:157]
	v_pk_add_f32 v[154:155], v[120:121], v[154:155]
	v_cvt_pk_bf16_f32 v206, v150, v151
	v_cvt_pk_bf16_f32 v207, v152, v153
	v_cvt_pk_bf16_f32 v208, v154, v155
	v_cvt_pk_bf16_f32 v209, v156, v157
	global_store_dwordx4 v[142:143], v[206:209], off
	v_mul_f32_e32 v151, v151, v151
	v_mul_f32_e32 v153, v153, v153
	v_mul_f32_e32 v155, v155, v155
	v_fmac_f32_e32 v151, v150, v150
	v_fmac_f32_e32 v153, v152, v152
	v_mul_f32_e32 v157, v157, v157
	v_fmac_f32_e32 v155, v154, v154
	v_add_f32_e32 v151, v151, v153
	v_fmac_f32_e32 v157, v156, v156
	v_add_f32_e32 v151, v151, v155
	v_add_f32_e32 v214, v157, v151
	s_waitcnt vmcnt(9)
	v_pk_add_f32 v[160:161], v[118:119], v[160:161]
	v_pk_add_f32 v[158:159], v[116:117], v[158:159]
	v_pk_add_f32 v[164:165], v[114:115], v[164:165]
	v_pk_add_f32 v[162:163], v[112:113], v[162:163]
	v_cvt_pk_bf16_f32 v210, v158, v159
	v_cvt_pk_bf16_f32 v211, v160, v161
	v_cvt_pk_bf16_f32 v212, v162, v163
	v_cvt_pk_bf16_f32 v213, v164, v165
	global_store_dwordx4 v[142:143], v[210:213], off offset:256
	v_mul_f32_e32 v159, v159, v159
	v_mul_f32_e32 v161, v161, v161
	v_mul_f32_e32 v163, v163, v163
	v_fmac_f32_e32 v159, v158, v158
	v_fmac_f32_e32 v161, v160, v160
	v_mul_f32_e32 v165, v165, v165
	v_fmac_f32_e32 v163, v162, v162
	v_add_f32_e32 v159, v159, v161
	v_fmac_f32_e32 v165, v164, v164
	v_add_f32_e32 v159, v159, v163
	v_add_f32_e32 v215, v165, v159
	v_add_f32_e32 v214, v214, v215
	s_mov_b64 s[98:99], 0x30000
	v_lshl_add_u64 v[202:203], v[140:141], 0, s[98:99]
	global_load_dwordx4 v[150:153], v[202:203], off nt
	global_load_dwordx4 v[154:157], v[202:203], off offset:16 nt
	global_load_dwordx4 v[158:161], v[202:203], off offset:512 nt
	global_load_dwordx4 v[162:165], v[202:203], off offset:528 nt
	v_mov_b32_e32 v215, v214
	s_nop 1
	v_permlane16_swap_b32_e32 v214, v215
	v_add_f32_e32 v214, v214, v215
	v_mov_b32_e32 v215, v214
	s_nop 1
	v_permlane32_swap_b32_e32 v214, v215
	s_and_saveexec_b64 s[16:17], s[2:3]
	v_add_f32_e32 v214, v214, v215
	ds_read_b32 v215, v147
	s_waitcnt lgkmcnt(0)
	v_add_f32_e32 v214, v214, v215
	ds_write_b32 v147, v214
	s_or_b64 exec, exec, s[16:17]
	s_waitcnt vmcnt(12)
	v_pk_add_f32 v[168:169], v[110:111], v[168:169]
	v_pk_add_f32 v[166:167], v[108:109], v[166:167]
	v_pk_add_f32 v[172:173], v[106:107], v[172:173]
	v_pk_add_f32 v[170:171], v[104:105], v[170:171]
	v_cvt_pk_bf16_f32 v206, v166, v167
	v_cvt_pk_bf16_f32 v207, v168, v169
	v_cvt_pk_bf16_f32 v208, v170, v171
	v_cvt_pk_bf16_f32 v209, v172, v173
	s_mov_b64 s[98:99], 0x8000
	v_lshl_add_u64 v[204:205], v[142:143], 0, s[98:99]
	global_store_dwordx4 v[204:205], v[206:209], off
	v_mul_f32_e32 v167, v167, v167
	v_mul_f32_e32 v169, v169, v169
	v_mul_f32_e32 v171, v171, v171
	v_fmac_f32_e32 v167, v166, v166
	v_fmac_f32_e32 v169, v168, v168
	v_mul_f32_e32 v173, v173, v173
	v_fmac_f32_e32 v171, v170, v170
	v_add_f32_e32 v167, v167, v169
	v_fmac_f32_e32 v173, v172, v172
	v_add_f32_e32 v167, v167, v171
	v_add_f32_e32 v214, v173, v167
	s_waitcnt vmcnt(11)
	v_pk_add_f32 v[176:177], v[102:103], v[176:177]
	v_pk_add_f32 v[174:175], v[100:101], v[174:175]
	v_pk_add_f32 v[180:181], v[98:99], v[180:181]
	v_pk_add_f32 v[178:179], v[96:97], v[178:179]
	v_cvt_pk_bf16_f32 v210, v174, v175
	v_cvt_pk_bf16_f32 v211, v176, v177
	v_cvt_pk_bf16_f32 v212, v178, v179
	v_cvt_pk_bf16_f32 v213, v180, v181
	global_store_dwordx4 v[204:205], v[210:213], off offset:256
	v_mul_f32_e32 v175, v175, v175
	v_mul_f32_e32 v177, v177, v177
	v_mul_f32_e32 v179, v179, v179
	v_fmac_f32_e32 v175, v174, v174
	v_fmac_f32_e32 v177, v176, v176
	v_mul_f32_e32 v181, v181, v181
	v_fmac_f32_e32 v179, v178, v178
	v_add_f32_e32 v175, v175, v177
	v_fmac_f32_e32 v181, v180, v180
	v_add_f32_e32 v175, v175, v179
	v_add_f32_e32 v215, v181, v175
	v_add_f32_e32 v214, v214, v215
	s_mov_b64 s[98:99], 0x80000
	v_lshl_add_u64 v[202:203], v[140:141], 0, s[98:99]
	global_load_dwordx4 v[166:169], v[202:203], off nt
	global_load_dwordx4 v[170:173], v[202:203], off offset:16 nt
	global_load_dwordx4 v[174:177], v[202:203], off offset:512 nt
	global_load_dwordx4 v[178:181], v[202:203], off offset:528 nt
	v_mov_b32_e32 v215, v214
	s_nop 1
	v_permlane16_swap_b32_e32 v214, v215
	v_add_f32_e32 v214, v214, v215
	v_mov_b32_e32 v215, v214
	s_nop 1
	v_permlane32_swap_b32_e32 v214, v215
	s_and_saveexec_b64 s[16:17], s[2:3]
	v_add_f32_e32 v214, v214, v215
	ds_read_b32 v215, v147 offset:256
	s_waitcnt lgkmcnt(0)
; #define PG8_LAS __attribute__((address_space(3)))
; __device__ __forceinline__ unsigned cvt_pk_bf16(float lo, float hi) { const f32x2c v = {lo, hi}; const bf16x2c b = __builtin_convertvector(v, bf16x2c); return __builtin_bit_cast(unsigned, b); }
;     __device__ __forceinline__ void operator()(const f32x4 (&acc)[2][2][4][2], const Unit& u, int wr, int wc, int fr, int fq) const {
;     ...
;             for (int m = 0; m < 4; ++m) { const size_t ro = (size_t)(row0 + ai * HALF + m * 16) * D + col0; float q = 0.f;
; #pragma unroll
;                 for (int bj = 0; bj < 2; ++bj) { const f32x4 v0 = acc[ai][bj][m][0] + *(const f32x4*)(R + ro + bj * HALF), v1 = acc[ai][bj][m][1] + *(const f32x4*)(R + ro + bj * HALF + 4);
;                     q += (v0[0] * v0[0] + v0[1] * v0[1]) + (v0[2] * v0[2] + v0[3] * v0[3]) + (v1[0] * v1[0] + v1[1] * v1[1]) + (v1[2] * v1[2] + v1[3] * v1[3]);
;                     u32x4 w; w.x = cvt_pk_bf16(v0[0], v0[1]); w.y = cvt_pk_bf16(v0[2], v0[3]); w.z = cvt_pk_bf16(v1[0], v1[1]); w.w = cvt_pk_bf16(v1[2], v1[3]);
;                     *(u32x4*)(O + ro + bj * HALF) = w; }
;                 q = rows_sum4(q);
;                 if (fq == 0) { PG8_LAS float* sp = ss + (ai * HALF + wr * 64 + m * 16 + fr) * 4 + wc; *sp += q; } }
	v_add_f32_e32 v214, v214, v215
	ds_write_b32 v147, v214 offset:256
	s_or_b64 exec, exec, s[16:17]
	s_waitcnt vmcnt(14)
	v_pk_add_f32 v[184:185], v[94:95], v[184:185]
	v_pk_add_f32 v[182:183], v[92:93], v[182:183]
	v_pk_add_f32 v[188:189], v[90:91], v[188:189]
	v_pk_add_f32 v[186:187], v[88:89], v[186:187]
	v_cvt_pk_bf16_f32 v206, v182, v183
	v_cvt_pk_bf16_f32 v207, v184, v185
	v_cvt_pk_bf16_f32 v208, v186, v187
	v_cvt_pk_bf16_f32 v209, v188, v189
	s_mov_b64 s[98:99], 0x10000
	v_lshl_add_u64 v[204:205], v[142:143], 0, s[98:99]
	global_store_dwordx4 v[204:205], v[206:209], off
	v_mul_f32_e32 v183, v183, v183
	v_mul_f32_e32 v185, v185, v185
	v_mul_f32_e32 v187, v187, v187
	v_fmac_f32_e32 v183, v182, v182
	v_fmac_f32_e32 v185, v184, v184
	v_mul_f32_e32 v189, v189, v189
	v_fmac_f32_e32 v187, v186, v186
	v_add_f32_e32 v183, v183, v185
	v_fmac_f32_e32 v189, v188, v188
	v_add_f32_e32 v183, v183, v187
	v_add_f32_e32 v214, v189, v183
	s_waitcnt vmcnt(13)
	v_pk_add_f32 v[192:193], v[86:87], v[192:193]
	v_pk_add_f32 v[190:191], v[84:85], v[190:191]
	v_pk_add_f32 v[200:201], v[82:83], v[200:201]
	v_pk_add_f32 v[198:199], v[80:81], v[198:199]
	v_cvt_pk_bf16_f32 v210, v190, v191
	v_cvt_pk_bf16_f32 v211, v192, v193
	v_cvt_pk_bf16_f32 v212, v198, v199
	v_cvt_pk_bf16_f32 v213, v200, v201
	global_store_dwordx4 v[204:205], v[210:213], off offset:256
	v_mul_f32_e32 v191, v191, v191
	v_mul_f32_e32 v193, v193, v193
	v_mul_f32_e32 v199, v199, v199
	v_fmac_f32_e32 v191, v190, v190
	v_fmac_f32_e32 v193, v192, v192
	v_mul_f32_e32 v201, v201, v201
	v_fmac_f32_e32 v199, v198, v198
	v_add_f32_e32 v191, v191, v193
	v_fmac_f32_e32 v201, v200, v200
	v_add_f32_e32 v191, v191, v199
	v_add_f32_e32 v215, v201, v191
	v_add_f32_e32 v214, v214, v215
	s_mov_b64 s[98:99], 0x90000
	v_lshl_add_u64 v[202:203], v[140:141], 0, s[98:99]
	global_load_dwordx4 v[182:185], v[202:203], off nt
	global_load_dwordx4 v[186:189], v[202:203], off offset:16 nt
	global_load_dwordx4 v[190:193], v[202:203], off offset:512 nt
	global_load_dwordx4 v[198:201], v[202:203], off offset:528 nt
	v_mov_b32_e32 v215, v214
	s_nop 1
	v_permlane16_swap_b32_e32 v214, v215
	v_add_f32_e32 v214, v214, v215
	v_mov_b32_e32 v215, v214
	s_nop 1
	v_permlane32_swap_b32_e32 v214, v215
	s_and_saveexec_b64 s[16:17], s[2:3]
	v_add_f32_e32 v214, v214, v215
	ds_read_b32 v215, v147 offset:512
	s_waitcnt lgkmcnt(0)
	v_add_f32_e32 v214, v214, v215
	ds_write_b32 v147, v214 offset:512
	s_or_b64 exec, exec, s[16:17]
	s_waitcnt vmcnt(14)
	v_pk_add_f32 v[152:153], v[78:79], v[152:153]
	v_pk_add_f32 v[150:151], v[76:77], v[150:151]
	v_pk_add_f32 v[156:157], v[74:75], v[156:157]
	v_pk_add_f32 v[154:155], v[72:73], v[154:155]
	v_cvt_pk_bf16_f32 v206, v150, v151
	v_cvt_pk_bf16_f32 v207, v152, v153
	v_cvt_pk_bf16_f32 v208, v154, v155
	v_cvt_pk_bf16_f32 v209, v156, v157
	s_mov_b64 s[98:99], 0x18000
	v_lshl_add_u64 v[204:205], v[142:143], 0, s[98:99]
	global_store_dwordx4 v[204:205], v[206:209], off
	v_mul_f32_e32 v151, v151, v151
	v_mul_f32_e32 v153, v153, v153
	v_mul_f32_e32 v155, v155, v155
	v_fmac_f32_e32 v151, v150, v150
	v_fmac_f32_e32 v153, v152, v152
	v_mul_f32_e32 v157, v157, v157
	v_fmac_f32_e32 v155, v154, v154
	v_add_f32_e32 v151, v151, v153
	v_fmac_f32_e32 v157, v156, v156
	v_add_f32_e32 v151, v151, v155
	v_add_f32_e32 v214, v157, v151
	s_waitcnt vmcnt(13)
	v_pk_add_f32 v[160:161], v[70:71], v[160:161]
	v_pk_add_f32 v[158:159], v[68:69], v[158:159]
	v_pk_add_f32 v[164:165], v[66:67], v[164:165]
	v_pk_add_f32 v[162:163], v[64:65], v[162:163]
	v_cvt_pk_bf16_f32 v210, v158, v159
	v_cvt_pk_bf16_f32 v211, v160, v161
	v_cvt_pk_bf16_f32 v212, v162, v163
	v_cvt_pk_bf16_f32 v213, v164, v165
	global_store_dwordx4 v[204:205], v[210:213], off offset:256
	v_mul_f32_e32 v159, v159, v159
	v_mul_f32_e32 v161, v161, v161
	v_mul_f32_e32 v163, v163, v163
	v_fmac_f32_e32 v159, v158, v158
	v_fmac_f32_e32 v161, v160, v160
	v_mul_f32_e32 v165, v165, v165
	v_fmac_f32_e32 v163, v162, v162
	v_add_f32_e32 v159, v159, v161
	v_fmac_f32_e32 v165, v164, v164
	v_add_f32_e32 v159, v159, v163
	v_add_f32_e32 v215, v165, v159
	v_add_f32_e32 v214, v214, v215
	s_mov_b64 s[98:99], 0xa0000
	v_lshl_add_u64 v[202:203], v[140:141], 0, s[98:99]
	global_load_dwordx4 v[150:153], v[202:203], off nt
	global_load_dwordx4 v[154:157], v[202:203], off offset:16 nt
	global_load_dwordx4 v[158:161], v[202:203], off offset:512 nt
	global_load_dwordx4 v[162:165], v[202:203], off offset:528 nt
	v_mov_b32_e32 v215, v214
	s_nop 1
	v_permlane16_swap_b32_e32 v214, v215
	v_add_f32_e32 v214, v214, v215
	v_mov_b32_e32 v215, v214
	s_nop 1
	v_permlane32_swap_b32_e32 v214, v215
	s_and_saveexec_b64 s[16:17], s[2:3]
	v_add_f32_e32 v214, v214, v215
	ds_read_b32 v215, v147 offset:768
	s_waitcnt lgkmcnt(0)
	v_add_f32_e32 v214, v214, v215
	ds_write_b32 v147, v214 offset:768
	s_or_b64 exec, exec, s[16:17]
	s_waitcnt vmcnt(14)
	v_pk_add_f32 v[168:169], v[62:63], v[168:169]
	v_pk_add_f32 v[166:167], v[60:61], v[166:167]
	v_pk_add_f32 v[172:173], v[58:59], v[172:173]
	v_pk_add_f32 v[170:171], v[56:57], v[170:171]
	v_cvt_pk_bf16_f32 v206, v166, v167
	v_cvt_pk_bf16_f32 v207, v168, v169
	v_cvt_pk_bf16_f32 v208, v170, v171
	v_cvt_pk_bf16_f32 v209, v172, v173
	s_mov_b64 s[98:99], 0x40000
	v_lshl_add_u64 v[204:205], v[142:143], 0, s[98:99]
	global_store_dwordx4 v[204:205], v[206:209], off
	v_mul_f32_e32 v167, v167, v167
	v_mul_f32_e32 v169, v169, v169
	v_mul_f32_e32 v171, v171, v171
	v_fmac_f32_e32 v167, v166, v166
	v_fmac_f32_e32 v169, v168, v168
	v_mul_f32_e32 v173, v173, v173
	v_fmac_f32_e32 v171, v170, v170
	v_add_f32_e32 v167, v167, v169
	v_fmac_f32_e32 v173, v172, v172
	v_add_f32_e32 v167, v167, v171
	v_add_f32_e32 v214, v173, v167
	s_waitcnt vmcnt(13)
; #define PG8_LAS __attribute__((address_space(3)))
; __device__ __forceinline__ unsigned cvt_pk_bf16(float lo, float hi) { const f32x2c v = {lo, hi}; const bf16x2c b = __builtin_convertvector(v, bf16x2c); return __builtin_bit_cast(unsigned, b); }
;     __device__ __forceinline__ void operator()(const f32x4 (&acc)[2][2][4][2], const Unit& u, int wr, int wc, int fr, int fq) const {
;     ...
;             for (int m = 0; m < 4; ++m) { const size_t ro = (size_t)(row0 + ai * HALF + m * 16) * D + col0; float q = 0.f;
; #pragma unroll
;                 for (int bj = 0; bj < 2; ++bj) { const f32x4 v0 = acc[ai][bj][m][0] + *(const f32x4*)(R + ro + bj * HALF), v1 = acc[ai][bj][m][1] + *(const f32x4*)(R + ro + bj * HALF + 4);
;                     q += (v0[0] * v0[0] + v0[1] * v0[1]) + (v0[2] * v0[2] + v0[3] * v0[3]) + (v1[0] * v1[0] + v1[1] * v1[1]) + (v1[2] * v1[2] + v1[3] * v1[3]);
;                     u32x4 w; w.x = cvt_pk_bf16(v0[0], v0[1]); w.y = cvt_pk_bf16(v0[2], v0[3]); w.z = cvt_pk_bf16(v1[0], v1[1]); w.w = cvt_pk_bf16(v1[2], v1[3]);
;                     *(u32x4*)(O + ro + bj * HALF) = w; }
;                 q = rows_sum4(q);
;                 if (fq == 0) { PG8_LAS float* sp = ss + (ai * HALF + wr * 64 + m * 16 + fr) * 4 + wc; *sp += q; } }
	v_pk_add_f32 v[176:177], v[54:55], v[176:177]
	v_pk_add_f32 v[174:175], v[52:53], v[174:175]
	v_pk_add_f32 v[180:181], v[50:51], v[180:181]
	v_pk_add_f32 v[178:179], v[48:49], v[178:179]
	v_cvt_pk_bf16_f32 v210, v174, v175
	v_cvt_pk_bf16_f32 v211, v176, v177
	v_cvt_pk_bf16_f32 v212, v178, v179
	v_cvt_pk_bf16_f32 v213, v180, v181
	global_store_dwordx4 v[204:205], v[210:213], off offset:256
	v_mul_f32_e32 v175, v175, v175
	v_mul_f32_e32 v177, v177, v177
	v_mul_f32_e32 v179, v179, v179
	v_fmac_f32_e32 v175, v174, v174
	v_fmac_f32_e32 v177, v176, v176
	v_mul_f32_e32 v181, v181, v181
	v_fmac_f32_e32 v179, v178, v178
	v_add_f32_e32 v175, v175, v177
	v_fmac_f32_e32 v181, v180, v180
	v_add_f32_e32 v175, v175, v179
	v_add_f32_e32 v215, v181, v175
	v_add_f32_e32 v214, v214, v215
	s_mov_b64 s[98:99], 0xb0000
	v_lshl_add_u64 v[202:203], v[140:141], 0, s[98:99]
	global_load_dwordx4 v[166:169], v[202:203], off nt
	global_load_dwordx4 v[170:173], v[202:203], off offset:16 nt
	global_load_dwordx4 v[174:177], v[202:203], off offset:512 nt
	global_load_dwordx4 v[178:181], v[202:203], off offset:528 nt
	v_mov_b32_e32 v215, v214
	s_nop 1
	v_permlane16_swap_b32_e32 v214, v215
	v_add_f32_e32 v214, v214, v215
	v_mov_b32_e32 v215, v214
	s_nop 1
	v_permlane32_swap_b32_e32 v214, v215
	s_and_saveexec_b64 s[16:17], s[2:3]
	v_add_f32_e32 v214, v214, v215
	ds_read_b32 v215, v147 offset:2048
	s_waitcnt lgkmcnt(0)
	v_add_f32_e32 v214, v214, v215
	ds_write_b32 v147, v214 offset:2048
	s_or_b64 exec, exec, s[16:17]
	s_waitcnt vmcnt(14)
	v_pk_add_f32 v[184:185], v[46:47], v[184:185]
	v_pk_add_f32 v[182:183], v[44:45], v[182:183]
	v_pk_add_f32 v[188:189], v[42:43], v[188:189]
	v_pk_add_f32 v[186:187], v[40:41], v[186:187]
	v_cvt_pk_bf16_f32 v206, v182, v183
	v_cvt_pk_bf16_f32 v207, v184, v185
	v_cvt_pk_bf16_f32 v208, v186, v187
	v_cvt_pk_bf16_f32 v209, v188, v189
	s_mov_b64 s[98:99], 0x48000
	v_lshl_add_u64 v[204:205], v[142:143], 0, s[98:99]
	global_store_dwordx4 v[204:205], v[206:209], off
	v_mul_f32_e32 v183, v183, v183
	v_mul_f32_e32 v185, v185, v185
	v_mul_f32_e32 v187, v187, v187
	v_fmac_f32_e32 v183, v182, v182
	v_fmac_f32_e32 v185, v184, v184
	v_mul_f32_e32 v189, v189, v189
	v_fmac_f32_e32 v187, v186, v186
	v_add_f32_e32 v183, v183, v185
	v_fmac_f32_e32 v189, v188, v188
	v_add_f32_e32 v183, v183, v187
	v_add_f32_e32 v214, v189, v183
	s_waitcnt vmcnt(13)
	v_pk_add_f32 v[192:193], v[38:39], v[192:193]
	v_pk_add_f32 v[190:191], v[36:37], v[190:191]
	v_pk_add_f32 v[200:201], v[34:35], v[200:201]
	v_pk_add_f32 v[198:199], v[32:33], v[198:199]
	v_cvt_pk_bf16_f32 v210, v190, v191
	v_cvt_pk_bf16_f32 v211, v192, v193
	v_cvt_pk_bf16_f32 v212, v198, v199
	v_cvt_pk_bf16_f32 v213, v200, v201
	global_store_dwordx4 v[204:205], v[210:213], off offset:256
	v_mul_f32_e32 v191, v191, v191
	v_mul_f32_e32 v193, v193, v193
	v_mul_f32_e32 v199, v199, v199
	v_fmac_f32_e32 v191, v190, v190
	v_fmac_f32_e32 v193, v192, v192
	v_mul_f32_e32 v201, v201, v201
	v_fmac_f32_e32 v199, v198, v198
	v_add_f32_e32 v191, v191, v193
	v_fmac_f32_e32 v201, v200, v200
	v_add_f32_e32 v191, v191, v199
	v_add_f32_e32 v215, v201, v191
	v_add_f32_e32 v214, v214, v215
	v_mov_b32_e32 v215, v214
	s_nop 1
	v_permlane16_swap_b32_e32 v214, v215
	v_add_f32_e32 v214, v214, v215
	v_mov_b32_e32 v215, v214
	s_nop 1
	v_permlane32_swap_b32_e32 v214, v215
	s_and_saveexec_b64 s[16:17], s[2:3]
	v_add_f32_e32 v214, v214, v215
	ds_read_b32 v215, v147 offset:2304
	s_waitcnt lgkmcnt(0)
	v_add_f32_e32 v214, v214, v215
	ds_write_b32 v147, v214 offset:2304
	s_or_b64 exec, exec, s[16:17]
	s_waitcnt vmcnt(10)
; #define PG8_LAS __attribute__((address_space(3)))
; __device__ __forceinline__ unsigned cvt_pk_bf16(float lo, float hi) { const f32x2c v = {lo, hi}; const bf16x2c b = __builtin_convertvector(v, bf16x2c); return __builtin_bit_cast(unsigned, b); }
;     __device__ __forceinline__ void operator()(const f32x4 (&acc)[2][2][4][2], const Unit& u, int wr, int wc, int fr, int fq) const {
;     ...
;             for (int m = 0; m < 4; ++m) { const size_t ro = (size_t)(row0 + ai * HALF + m * 16) * D + col0; float q = 0.f;
; #pragma unroll
;                 for (int bj = 0; bj < 2; ++bj) { const f32x4 v0 = acc[ai][bj][m][0] + *(const f32x4*)(R + ro + bj * HALF), v1 = acc[ai][bj][m][1] + *(const f32x4*)(R + ro + bj * HALF + 4);
;                     q += (v0[0] * v0[0] + v0[1] * v0[1]) + (v0[2] * v0[2] + v0[3] * v0[3]) + (v1[0] * v1[0] + v1[1] * v1[1]) + (v1[2] * v1[2] + v1[3] * v1[3]);
;                     u32x4 w; w.x = cvt_pk_bf16(v0[0], v0[1]); w.y = cvt_pk_bf16(v0[2], v0[3]); w.z = cvt_pk_bf16(v1[0], v1[1]); w.w = cvt_pk_bf16(v1[2], v1[3]);
;                     *(u32x4*)(O + ro + bj * HALF) = w; }
;                 q = rows_sum4(q);
;                 if (fq == 0) { PG8_LAS float* sp = ss + (ai * HALF + wr * 64 + m * 16 + fr) * 4 + wc; *sp += q; } }
	v_pk_add_f32 v[152:153], v[30:31], v[152:153]
	v_pk_add_f32 v[150:151], v[28:29], v[150:151]
	v_pk_add_f32 v[156:157], v[26:27], v[156:157]
	v_pk_add_f32 v[154:155], v[24:25], v[154:155]
	v_cvt_pk_bf16_f32 v206, v150, v151
	v_cvt_pk_bf16_f32 v207, v152, v153
	v_cvt_pk_bf16_f32 v208, v154, v155
	v_cvt_pk_bf16_f32 v209, v156, v157
	s_mov_b64 s[98:99], 0x50000
	v_lshl_add_u64 v[204:205], v[142:143], 0, s[98:99]
	global_store_dwordx4 v[204:205], v[206:209], off
	v_mul_f32_e32 v151, v151, v151
	v_mul_f32_e32 v153, v153, v153
	v_mul_f32_e32 v155, v155, v155
	v_fmac_f32_e32 v151, v150, v150
	v_fmac_f32_e32 v153, v152, v152
	v_mul_f32_e32 v157, v157, v157
	v_fmac_f32_e32 v155, v154, v154
	v_add_f32_e32 v151, v151, v153
	v_fmac_f32_e32 v157, v156, v156
	v_add_f32_e32 v151, v151, v155
	v_add_f32_e32 v214, v157, v151
	s_waitcnt vmcnt(9)
	v_pk_add_f32 v[160:161], v[22:23], v[160:161]
	v_pk_add_f32 v[158:159], v[20:21], v[158:159]
	v_pk_add_f32 v[164:165], v[18:19], v[164:165]
	v_pk_add_f32 v[162:163], v[16:17], v[162:163]
	v_cvt_pk_bf16_f32 v210, v158, v159
	v_cvt_pk_bf16_f32 v211, v160, v161
	v_cvt_pk_bf16_f32 v212, v162, v163
	v_cvt_pk_bf16_f32 v213, v164, v165
	global_store_dwordx4 v[204:205], v[210:213], off offset:256
	v_mul_f32_e32 v159, v159, v159
	v_mul_f32_e32 v161, v161, v161
	v_mul_f32_e32 v163, v163, v163
	v_fmac_f32_e32 v159, v158, v158
	v_fmac_f32_e32 v161, v160, v160
	v_mul_f32_e32 v165, v165, v165
	v_fmac_f32_e32 v163, v162, v162
	v_add_f32_e32 v159, v159, v161
	v_fmac_f32_e32 v165, v164, v164
	v_add_f32_e32 v159, v159, v163
	v_add_f32_e32 v215, v165, v159
	v_add_f32_e32 v214, v214, v215
	v_mov_b32_e32 v215, v214
	s_nop 1
	v_permlane16_swap_b32_e32 v214, v215
	v_add_f32_e32 v214, v214, v215
	v_mov_b32_e32 v215, v214
	s_nop 1
	v_permlane32_swap_b32_e32 v214, v215
	s_and_saveexec_b64 s[16:17], s[2:3]
	v_add_f32_e32 v214, v214, v215
	ds_read_b32 v215, v147 offset:2560
	s_waitcnt lgkmcnt(0)
	v_add_f32_e32 v214, v214, v215
	ds_write_b32 v147, v214 offset:2560
	s_or_b64 exec, exec, s[16:17]
	s_waitcnt vmcnt(6)
	v_pk_add_f32 v[168:169], v[14:15], v[168:169]
	v_pk_add_f32 v[166:167], v[12:13], v[166:167]
	v_pk_add_f32 v[172:173], v[10:11], v[172:173]
	v_pk_add_f32 v[170:171], v[8:9], v[170:171]
	v_cvt_pk_bf16_f32 v206, v166, v167
	v_cvt_pk_bf16_f32 v207, v168, v169
	v_cvt_pk_bf16_f32 v208, v170, v171
	v_cvt_pk_bf16_f32 v209, v172, v173
	s_mov_b64 s[98:99], 0x58000
	v_lshl_add_u64 v[204:205], v[142:143], 0, s[98:99]
	global_store_dwordx4 v[204:205], v[206:209], off
	v_mul_f32_e32 v167, v167, v167
	v_mul_f32_e32 v169, v169, v169
	v_mul_f32_e32 v171, v171, v171
	v_fmac_f32_e32 v167, v166, v166
	v_fmac_f32_e32 v169, v168, v168
	v_mul_f32_e32 v173, v173, v173
	v_fmac_f32_e32 v171, v170, v170
	v_add_f32_e32 v167, v167, v169
	v_fmac_f32_e32 v173, v172, v172
	v_add_f32_e32 v167, v167, v171
	v_add_f32_e32 v214, v173, v167
	s_waitcnt vmcnt(5)
	v_pk_add_f32 v[176:177], v[6:7], v[176:177]
	v_pk_add_f32 v[174:175], v[4:5], v[174:175]
	v_pk_add_f32 v[180:181], v[2:3], v[180:181]
	v_pk_add_f32 v[178:179], v[0:1], v[178:179]
	v_cvt_pk_bf16_f32 v210, v174, v175
	v_cvt_pk_bf16_f32 v211, v176, v177
	v_cvt_pk_bf16_f32 v212, v178, v179
	v_cvt_pk_bf16_f32 v213, v180, v181
	global_store_dwordx4 v[204:205], v[210:213], off offset:256
	v_mul_f32_e32 v175, v175, v175
	v_mul_f32_e32 v177, v177, v177
	v_mul_f32_e32 v179, v179, v179
	v_fmac_f32_e32 v175, v174, v174
	v_fmac_f32_e32 v177, v176, v176
	v_mul_f32_e32 v181, v181, v181
	v_fmac_f32_e32 v179, v178, v178
	v_add_f32_e32 v175, v175, v177
	v_fmac_f32_e32 v181, v180, v180
	v_add_f32_e32 v175, v175, v179
	v_add_f32_e32 v215, v181, v175
	v_add_f32_e32 v214, v214, v215
	v_mov_b32_e32 v215, v214
	s_nop 1
	v_permlane16_swap_b32_e32 v214, v215
	v_add_f32_e32 v214, v214, v215
	v_mov_b32_e32 v215, v214
	s_nop 1
	v_permlane32_swap_b32_e32 v214, v215
	s_and_saveexec_b64 s[16:17], s[2:3]
	v_add_f32_e32 v214, v214, v215
	ds_read_b32 v215, v147 offset:2816
	s_waitcnt lgkmcnt(0)
	v_add_f32_e32 v214, v214, v215
	ds_write_b32 v147, v214 offset:2816
	s_or_b64 exec, exec, s[16:17]
	s_cmp_eq_u32 s61, 3
	s_mov_b64 s[16:17], -1
	s_cbranch_scc1 .LBB0_2032
	s_andn2_b64 vcc, exec, s[4:5]
	s_cbranch_vccnz .LBB0_2031
	s_barrier
	s_branch .LBB0_2031
